# layer-0 w_in phase re-split: 142 conversion workgroups / 114 GEMM workgroups (was 152/104) so the GEMM takes 9 rounds instead of 10; all 45 literals of the conversion code that embed the conversion wo
# baseline (speedup 1.0000x reference)
.LBB0_102:
	s_load_dwordx16 s[36:51], s[0:1], 0x40
	s_add_u32 s30, s16, 0x100000
	s_addc_u32 s31, s17, 0
	s_add_u32 s26, s16, 0x25313200
	s_addc_u32 s27, s17, 0
	s_waitcnt lgkmcnt(0)
	v_writelane_b32 v251, s36, 31
	s_cmpk_lt_i32 s96, 0x80
	s_cselect_b64 s[0:1], -1, 0
	v_writelane_b32 v251, s37, 32
	v_writelane_b32 v251, s38, 33
	v_writelane_b32 v251, s39, 34
	v_writelane_b32 v251, s40, 35
	v_writelane_b32 v251, s41, 36
	v_writelane_b32 v251, s42, 37
	v_writelane_b32 v251, s43, 38
	v_writelane_b32 v251, s44, 39
	v_writelane_b32 v251, s45, 40
	v_writelane_b32 v251, s46, 41
	v_writelane_b32 v251, s47, 42
	v_writelane_b32 v251, s48, 43
	v_writelane_b32 v251, s49, 44
	v_writelane_b32 v251, s50, 45
	v_writelane_b32 v251, s51, 46
	v_writelane_b32 v251, s0, 47
	v_mov_b32_e32 v3, 0
	v_mbcnt_lo_u32_b32 v1, -1, 0
	v_writelane_b32 v251, s1, 48
	s_lshr_b32 s0, s96, 31
	s_add_i32 s0, s96, s0
	s_lshl_b32 s1, s0, 6
	s_and_b32 s1, s1, 0xffffff80
	s_and_b32 s0, s0, -2
	s_sub_i32 s2, s96, s0
	v_writelane_b32 v251, s1, 49
	s_add_i32 s0, s1, 0x80
	v_writelane_b32 v251, s0, 50
	s_mov_b32 s0, s2
	s_ashr_i32 s3, s2, 31
	v_writelane_b32 v251, s0, 51
	v_mov_b32_e32 v228, 1
	v_mbcnt_hi_u32_b32 v229, -1, v1
	v_writelane_b32 v251, s1, 52
	s_lshl_b64 s[0:1], s[2:3], 20
	s_add_u32 s0, s26, s0
	s_addc_u32 s1, s27, s1
	s_add_u32 s2, s0, 0x4000
	s_addc_u32 s3, s1, 0
	v_writelane_b32 v251, s2, 53
	v_mov_b32_e32 v230, 0x358637bd
	v_mov_b32_e32 v231, 0x260
	v_writelane_b32 v251, s3, 54
	s_add_u32 s2, s0, 0x8000
	s_addc_u32 s3, s1, 0
	v_writelane_b32 v251, s2, 55
	v_mov_b32_e32 v232, 0x3727c5ac
	v_mov_b64_e32 v[202:203], 0xff
	v_writelane_b32 v251, s3, 56
	s_add_u32 s2, s16, 0x100080
	s_addc_u32 s3, s17, 0
	v_writelane_b32 v251, s2, 57
	v_mov_b32_e32 v233, 0x41b17218
	v_mov_b32_e32 v234, 0xf149f2ca
	v_writelane_b32 v251, s3, 58
	s_add_u32 s2, s0, 0xc000
	v_writelane_b32 v251, s0, 59
	s_addc_u32 s3, s1, 0
	v_mov_b32_e32 v235, 0x2200
	v_writelane_b32 v251, s1, 60
	v_writelane_b32 v251, s2, 61
	s_add_u32 s0, s16, 0x6102200
	s_addc_u32 s1, s17, 0
	v_writelane_b32 v251, s3, 62
	v_writelane_b32 v251, s0, 63
	v_mov_b32_e32 v84, v3
	v_mov_b32_e32 v85, v3
	v_writelane_b32 v252, s1, 0
	s_add_u32 s0, s16, 0x25514300
	v_writelane_b32 v252, s0, 1
	s_addc_u32 s0, s17, 0
	s_cmpk_lt_i32 s66, 0x100
	v_writelane_b32 v252, s0, 2
	s_cselect_b64 s[0:1], -1, 0
	v_writelane_b32 v252, s0, 3
	v_mov_b32_e32 v86, v3
	v_mov_b32_e32 v87, v3
	v_writelane_b32 v252, s1, 4
	s_ashr_i32 s0, s66, 31
	v_writelane_b32 v252, s0, 5
	s_lshr_b32 s0, s0, 29
	s_add_i32 s0, s66, s0
	s_ashr_i32 s2, s0, 3
	s_and_b32 s0, s0, -8
	s_sub_i32 s3, s66, s0
	s_lshl_b32 s4, s3, 5
	s_add_u32 s0, s16, 0x4200
	s_addc_u32 s1, s17, 0
	v_writelane_b32 v252, s0, 6
	v_mov_b32_e32 v236, 0x2000880
	v_mov_b32_e32 v237, 0x1000
	v_writelane_b32 v252, s1, 7
	s_add_u32 s0, s16, 0x4400
	s_addc_u32 s1, s17, 0
	v_writelane_b32 v252, s0, 8
	v_mov_b32_e32 v238, 0x1800
	s_movk_i32 s29, 0x80
	v_writelane_b32 v252, s1, 9
	s_add_u32 s0, s16, 0x4500
	s_addc_u32 s1, s17, 0
	v_writelane_b32 v252, s0, 10
	s_mov_b32 s90, 0
	s_mov_b32 s35, 0
	v_writelane_b32 v252, s1, 11
	s_add_u32 s0, s16, 0x4600
	s_addc_u32 s1, s17, 0
	v_writelane_b32 v252, s0, 12
	s_mov_b64 s[36:37], 0x80
	s_mov_b32 s46, 0x3e38aa3b
	v_writelane_b32 v252, s1, 13
	s_add_u32 s0, s16, 0x4700
	s_addc_u32 s1, s17, 0
	v_writelane_b32 v252, s0, 14
	s_mov_b32 s28, 0x3fd744fd
	s_nop 0
	v_writelane_b32 v252, s1, 15
	s_add_u32 s0, s16, 0x4800
	s_addc_u32 s1, s17, 0
	v_writelane_b32 v252, s0, 16
	s_nop 1
	v_writelane_b32 v252, s1, 17
	s_add_u32 s0, s16, 0x4900
	s_addc_u32 s1, s17, 0
	v_writelane_b32 v252, s0, 18
	s_nop 1
	v_writelane_b32 v252, s1, 19
	s_add_u32 s0, s16, 0x4a00
	s_addc_u32 s1, s17, 0
	v_writelane_b32 v252, s0, 20
	s_nop 1
	v_writelane_b32 v252, s1, 21
	s_add_u32 s0, s16, 0x4b00
	s_addc_u32 s1, s17, 0
	v_writelane_b32 v252, s0, 22
	s_nop 1
	v_writelane_b32 v252, s1, 23
	s_add_u32 s0, s16, 0x4c00
	s_addc_u32 s1, s17, 0
	v_writelane_b32 v252, s0, 24
	s_nop 1
	v_writelane_b32 v252, s1, 25
	s_add_u32 s0, s16, 0x4d00
	s_addc_u32 s1, s17, 0
	v_writelane_b32 v252, s0, 26
	s_nop 1
	v_writelane_b32 v252, s1, 27
	s_add_u32 s0, s16, 0x4e00
	s_addc_u32 s1, s17, 0
	v_writelane_b32 v252, s0, 28
	s_nop 1
	v_writelane_b32 v252, s1, 29
	s_add_u32 s0, s16, 0x4f00
	s_addc_u32 s1, s17, 0
	v_writelane_b32 v252, s0, 30
	s_nop 1
	v_writelane_b32 v252, s1, 31
	s_add_u32 s0, s16, 0x5000
	s_addc_u32 s1, s17, 0
	v_writelane_b32 v252, s0, 32
	s_nop 1
	v_writelane_b32 v252, s1, 33
	s_add_u32 s0, s16, 0x5100
	s_addc_u32 s1, s17, 0
	v_writelane_b32 v252, s0, 34
	s_nop 1
	v_writelane_b32 v252, s1, 35
	s_add_u32 s0, s16, 0x5200
	s_addc_u32 s1, s17, 0
	v_writelane_b32 v252, s0, 36
	s_nop 1
	v_writelane_b32 v252, s1, 37
	s_add_u32 s0, s16, 0x5300
	s_addc_u32 s1, s17, 0
	v_writelane_b32 v252, s0, 38
	s_cmp_eq_u32 s33, 15
	s_nop 0
	v_writelane_b32 v252, s1, 39
	s_cselect_b64 s[0:1], -1, 0
	v_writelane_b32 v252, s0, 40
	s_cmp_eq_u32 s33, 14
	s_nop 0
	v_writelane_b32 v252, s1, 41
	s_cselect_b64 s[0:1], -1, 0
	v_writelane_b32 v252, s0, 42
	s_cmp_eq_u32 s33, 13
	s_nop 0
	v_writelane_b32 v252, s1, 43
	s_cselect_b64 s[0:1], -1, 0
	v_writelane_b32 v252, s0, 44
	s_cmp_eq_u32 s33, 12
	s_nop 0
	v_writelane_b32 v252, s1, 45
	s_cselect_b64 s[0:1], -1, 0
	v_writelane_b32 v252, s0, 46
	s_cmp_eq_u32 s33, 11
	s_nop 0
	v_writelane_b32 v252, s1, 47
	s_cselect_b64 s[0:1], -1, 0
	v_writelane_b32 v252, s0, 48
	s_cmp_eq_u32 s33, 10
	s_nop 0
	v_writelane_b32 v252, s1, 49
	s_cselect_b64 s[0:1], -1, 0
	v_writelane_b32 v252, s0, 50
	s_cmp_eq_u32 s33, 9
	s_nop 0
	v_writelane_b32 v252, s1, 51
	s_cselect_b64 s[0:1], -1, 0
	v_writelane_b32 v252, s0, 52
	s_cmp_eq_u32 s33, 8
	s_nop 0
	v_writelane_b32 v252, s1, 53
	s_cselect_b64 s[0:1], -1, 0
	v_writelane_b32 v252, s0, 54
	s_cmp_eq_u32 s33, 7
	s_nop 0
	v_writelane_b32 v252, s1, 55
	s_cselect_b64 s[0:1], -1, 0
	v_writelane_b32 v252, s0, 56
	s_cmp_eq_u32 s33, 6
	s_nop 0
	v_writelane_b32 v252, s1, 57
	s_cselect_b64 s[0:1], -1, 0
	v_writelane_b32 v252, s0, 58
	s_cmp_eq_u32 s33, 5
	s_nop 0
	v_writelane_b32 v252, s1, 59
	s_cselect_b64 s[0:1], -1, 0
	v_writelane_b32 v252, s0, 60
	s_cmp_eq_u32 s33, 4
	s_nop 0
	v_writelane_b32 v252, s1, 61
	s_cselect_b64 s[0:1], -1, 0
	v_writelane_b32 v252, s0, 62
	s_cmp_eq_u32 s33, 3
	s_nop 0
	v_writelane_b32 v252, s1, 63
	s_cselect_b64 s[0:1], -1, 0
	v_writelane_b32 v253, s0, 0
	s_cmp_eq_u32 s33, 2
	s_nop 0
	v_writelane_b32 v253, s1, 1
	s_cselect_b64 s[0:1], -1, 0
	v_writelane_b32 v253, s0, 2
	s_cmp_eq_u32 s33, 1
	s_nop 0
	v_writelane_b32 v253, s1, 3
	s_cselect_b64 s[0:1], -1, 0
	v_writelane_b32 v253, s0, 4
	s_cmp_eq_u32 s33, 0
	s_nop 0
	v_writelane_b32 v253, s1, 5
	s_cselect_b64 s[0:1], -1, 0
	v_writelane_b32 v253, s0, 6
	s_nop 1
	v_writelane_b32 v253, s1, 7
	s_lshl_b32 s0, s33, 8
	s_add_u32 s0, s14, s0
	s_addc_u32 s1, s15, 0
	s_add_u32 s6, s0, 0x1400
	s_addc_u32 s7, s1, 0
	v_writelane_b32 v253, s6, 8
	s_add_u32 s0, s0, 0x2400
	s_addc_u32 s1, s1, 0
	v_writelane_b32 v253, s7, 9
	v_writelane_b32 v253, s0, 10
	s_nop 1
	v_writelane_b32 v253, s1, 11
	s_add_u32 s0, s16, 0x7400
	s_addc_u32 s1, s17, 0
	v_writelane_b32 v253, s0, 12
	s_nop 1
	v_writelane_b32 v253, s1, 13
	s_add_u32 s0, s16, 0x7500
	s_addc_u32 s1, s17, 0
	v_writelane_b32 v253, s0, 14
	s_nop 1
	v_writelane_b32 v253, s1, 15
	s_add_u32 s0, s16, 0x1a10aa00
	s_addc_u32 s1, s17, 0
	v_writelane_b32 v253, s0, 16
	s_nop 1
	v_writelane_b32 v253, s1, 17
	s_add_u32 s0, s16, 0x1a50bb00
	s_addc_u32 s1, s17, 0
	v_writelane_b32 v253, s0, 18
	s_cmpk_lt_i32 s96, 0x100
	s_nop 0
	v_writelane_b32 v253, s1, 19
	s_cselect_b64 s[0:1], -1, 0
	v_writelane_b32 v253, s0, 20
	s_nop 1
	v_writelane_b32 v253, s1, 21
	s_add_u32 s0, s16, 0x16108800
	s_addc_u32 s1, s17, 0
	s_add_u32 s78, s16, 0x18109900
	s_addc_u32 s79, s17, 0
	s_add_u32 s5, s16, 0x26515400
	v_writelane_b32 v253, s5, 22
	s_addc_u32 s5, s17, 0
	s_add_u32 s6, s16, 0x16108880
	v_writelane_b32 v253, s5, 23
	s_addc_u32 s7, s17, 0
	s_add_i32 s5, s20, 0xffffff72
	v_writelane_b32 v253, s6, 24
	s_cmp_lt_i32 s66, s5
	s_nop 0
	v_writelane_b32 v253, s7, 25
	s_cselect_b64 s[6:7], -1, 0
	v_writelane_b32 v253, s6, 26
	s_nop 1
	v_writelane_b32 v253, s7, 27
	v_writelane_b32 v253, s5, 28
	s_sub_i32 s5, s66, s5
	s_lshl_b32 s6, s5, 3
	v_writelane_b32 v253, s6, 29
	s_add_u32 s6, s16, 0x20311000
	v_writelane_b32 v253, s6, 30
	s_addc_u32 s6, s17, 0
	v_writelane_b32 v253, s6, 31
	s_add_u32 s6, s16, 0x24312100
	v_writelane_b32 v253, s6, 32
	s_addc_u32 s6, s17, 0
	v_writelane_b32 v253, s6, 33
	s_add_u32 s6, s16, 0x27516500
	v_writelane_b32 v253, s6, 34
	s_addc_u32 s6, s17, 0
	v_writelane_b32 v253, s6, 35
	s_add_u32 s6, s16, 0x47517600
	v_writelane_b32 v253, s6, 36
	s_addc_u32 s6, s17, 0
	v_writelane_b32 v253, s6, 37
	s_add_u32 s6, s16, 0x5f61ba00
	s_addc_u32 s7, s17, 0
	v_writelane_b32 v253, s6, 38
	s_lshl_b32 s5, s5, 9
	s_cmpk_lt_i32 s66, 0x400
	v_writelane_b32 v253, s7, 39
	v_writelane_b32 v253, s5, 40
	s_cselect_b64 s[6:7], -1, 0
	v_writelane_b32 v253, s6, 41
	s_lshl_b32 s5, s3, 7
	s_nop 0
	v_writelane_b32 v253, s7, 42
	s_add_u32 s6, s16, 0x8103300
	s_addc_u32 s7, s17, 0
	s_add_u32 s10, s16, 0xa104400
	v_writelane_b32 v253, s6, 43
	s_addc_u32 s11, s17, 0
	s_nop 0
	v_writelane_b32 v253, s7, 44
	s_add_u32 s6, s16, 0x12107700
	s_addc_u32 s7, s17, 0
	v_writelane_b32 v253, s6, 45
	s_nop 1
	v_writelane_b32 v253, s7, 46
	s_add_u32 s6, s16, 0x57518700
	s_addc_u32 s7, s17, 0
	v_writelane_b32 v253, s6, 47
	s_nop 1
	v_writelane_b32 v253, s7, 48
	s_add_u32 s6, s16, 0x5f51a900
	s_addc_u32 s7, s17, 0
	v_writelane_b32 v253, s6, 49
	s_cmpk_lt_i32 s96, 0x800
	s_nop 0
	v_writelane_b32 v253, s7, 50
	s_cselect_b64 s[6:7], -1, 0
	v_writelane_b32 v253, s6, 51
	s_lshl_b32 s9, s96, 13
	s_and_b32 s9, s9, 0x3e0000
	v_writelane_b32 v253, s7, 52
	s_lshl_b32 s6, s96, 7
	s_and_b32 s8, s6, 0x780
	s_ashr_i32 s6, s96, 9
	s_ashr_i32 s7, s6, 31
	s_lshl_b64 s[6:7], s[6:7], 22
	s_or_b32 s6, s6, s9
	s_or_b32 s6, s6, s8
	v_writelane_b32 v253, s6, 53
	s_nop 1
	v_writelane_b32 v253, s7, 54
	s_lshl_b64 s[6:7], s[6:7], 1
	v_writelane_b32 v253, s10, 55
	s_add_u32 s6, s10, s6
	v_writelane_b32 v253, s11, 56
	s_addc_u32 s7, s11, s7
	v_writelane_b32 v253, s6, 57
	s_nop 1
	v_writelane_b32 v253, s7, 58
	s_add_u32 s6, s16, 0x5b519800
	s_addc_u32 s7, s17, 0
	v_writelane_b32 v253, s6, 59
	s_nop 1
	v_writelane_b32 v253, s7, 60
	s_lshl_b32 s6, s96, 9
	v_writelane_b32 v253, s6, 61
	s_lshl_b32 s6, s20, 9
	v_writelane_b32 v253, s6, 62
	s_add_u32 s6, s16, 0xc105500
	s_addc_u32 s7, s17, 0
	v_writelane_b32 v253, s6, 63
	s_cmpk_lt_i32 s96, 0x400
	s_nop 0
	v_writelane_b32 v254, s7, 0
	s_cselect_b64 s[6:7], -1, 0
	v_writelane_b32 v254, s6, 1
	s_nop 1
	v_writelane_b32 v254, s7, 2
	s_lshl_b32 s6, s96, 4
	v_writelane_b32 v254, s6, 3
	s_and_b32 s6, s6, 0xf0
	s_and_b32 s7, s96, 0x7fffff00
	s_or_b32 s6, s7, s6
	s_bfe_u32 s7, s96, 0x40004
	s_or_b32 s6, s6, s7
	s_lshl_b32 s6, s6, 1
	s_add_u32 s22, s16, 0x4101100
	s_addc_u32 s23, s17, 0
	v_writelane_b32 v254, s6, 4
	s_add_u32 s6, s16, 0x6381dc00
	s_addc_u32 s7, s17, 0
	v_writelane_b32 v254, s6, 5
	s_nop 1
	v_writelane_b32 v254, s7, 6
	s_add_u32 s6, s16, 0x1a90cc00
	s_addc_u32 s7, s17, 0
	v_writelane_b32 v254, s6, 7
	s_nop 1
	v_writelane_b32 v254, s7, 8
	s_add_u32 s6, s16, 0x1aa0dd00
	s_addc_u32 s7, s17, 0
	v_writelane_b32 v254, s6, 9
	s_lshl_b32 s8, s96, 5
	s_nop 0
	v_writelane_b32 v254, s7, 10
	s_ashr_i32 s6, s20, 31
	s_lshr_b32 s6, s6, 30
	s_add_i32 s6, s20, s6
	s_ashr_i32 s6, s6, 2
	v_writelane_b32 v254, s6, 11
	s_add_u32 s6, s16, 0x10000
	v_writelane_b32 v254, s6, 12
	s_addc_u32 s6, s17, 0
	s_lshl_b32 s7, s20, 1
	v_writelane_b32 v254, s6, 13
	s_add_i32 s9, s96, s7
	v_writelane_b32 v254, s7, 14
	s_ashr_i32 s7, s9, 31
	s_ashr_i32 s6, s96, 31
	s_lshr_b32 s7, s7, 30
	s_lshr_b32 s6, s6, 30
	s_add_i32 s7, s9, s7
	s_add_i32 s6, s96, s6
	v_writelane_b32 v254, s9, 15
	s_ashr_i32 s7, s7, 2
	v_writelane_b32 v254, s7, 16
	s_ashr_i32 s7, s6, 2
	s_add_u32 s24, s16, 0x1ab0ee00
	s_addc_u32 s25, s17, 0
	s_add_u32 s10, s16, 0x6391ed00
	v_writelane_b32 v254, s7, 17
	s_addc_u32 s11, s17, 0
	v_writelane_b32 v254, s10, 18
	s_and_b32 s6, s6, -4
	s_sub_i32 s6, s96, s6
	v_writelane_b32 v254, s11, 19
	v_writelane_b32 v254, s6, 20
	s_add_u32 s6, s16, 0x4101180
	s_addc_u32 s7, s17, 0
	v_writelane_b32 v254, s6, 21
	s_nop 1
	v_writelane_b32 v254, s7, 22
	s_add_u32 s6, s16, 0x1c30ff00
	s_addc_u32 s7, s17, 0
	v_writelane_b32 v254, s6, 23
	s_nop 1
	v_writelane_b32 v254, s7, 24
	s_add_u32 s6, s16, 0x1ab0ee80
	s_addc_u32 s7, s17, 0
	v_writelane_b32 v254, s6, 25
	s_nop 1
	v_writelane_b32 v254, s7, 26
	s_add_u32 s6, s16, 0x1e310780
	s_addc_u32 s7, s17, 0
	v_writelane_b32 v254, s6, 27
	s_cmp_lt_i32 s3, 0
	s_nop 0
	v_writelane_b32 v254, s7, 28
	s_mul_i32 s6, s3, 33
	s_cselect_b32 s4, s6, s4
	s_mulk_i32 s3, 0x81
	s_cselect_b32 s3, s3, s5
	s_add_i32 s4, s4, s2
	s_ashr_i32 s5, s4, 31
	s_lshr_b32 s5, s5, 26
	s_add_i32 s5, s4, s5
	s_and_b32 s6, s5, 0xffc0
	s_sub_i32 s4, s4, s6
	s_bfe_i32 s6, s4, 0x80000
	s_bfe_u32 s6, s6, 0x3000c
	s_add_i32 s6, s4, s6
	s_and_b32 s7, s6, 0xf8
	s_add_i32 s2, s3, s2
	s_sub_i32 s4, s4, s7
	s_ashr_i32 s3, s2, 31
	s_sext_i32_i8 s4, s4
	s_lshl_b32 s5, s5, 5
	s_lshr_b32 s3, s3, 24
	s_and_b32 s5, s5, 0xfffff800
	s_lshl_b32 s4, s4, 8
	s_add_i32 s3, s2, s3
	s_add_i32 s7, s4, s5
	s_and_b32 s4, s3, 0xff00
	s_sub_i32 s2, s2, s4
	s_sext_i32_i16 s4, s2
	s_bfe_u32 s4, s4, 0x3001c
	s_add_i32 s4, s2, s4
	s_and_b32 s5, s4, 0xfff8
	s_sub_i32 s2, s2, s5
	s_sext_i32_i16 s2, s2
	s_lshl_b32 s3, s3, 3
	s_and_b32 s3, s3, 0xfffff800
	s_lshl_b32 s2, s2, 8
	s_add_i32 s5, s2, s3
	s_bfe_i32 s2, s6, 0x80000
	s_sext_i32_i16 s2, s2
	s_ashr_i32 s3, s2, 3
	s_lshr_b32 s2, s2, 3
	v_writelane_b32 v254, s3, 29
	s_bfe_i64 s[2:3], s[2:3], 0x100000
	s_lshl_b64 s[2:3], s[2:3], 20
	v_writelane_b32 v254, s2, 30
	s_nop 1
	v_writelane_b32 v254, s3, 31
	s_sext_i32_i16 s2, s4
	s_ashr_i32 s3, s2, 3
	s_lshr_b32 s2, s2, 3
	v_writelane_b32 v254, s3, 32
	s_bfe_i64 s[2:3], s[2:3], 0x100000
	s_lshl_b64 s[2:3], s[2:3], 20
	v_writelane_b32 v254, s2, 33
	s_nop 1
	v_writelane_b32 v254, s3, 34
	v_writelane_b32 v254, s7, 35
	s_or_b32 s2, s7, 0x80
	v_writelane_b32 v254, s2, 36
	v_writelane_b32 v254, s5, 37
	s_or_b32 s2, s5, 0x80
	v_writelane_b32 v254, s2, 38
	s_lshl_b32 s2, s20, 5
	v_writelane_b32 v254, s2, 39
	s_lshl_b32 s2, s96, 12
	v_writelane_b32 v254, s2, 40
	s_lshl_b32 s2, s20, 12
	v_writelane_b32 v254, s2, 41
	s_lshl_b32 s2, s20, 4
	v_writelane_b32 v254, s2, 42
	v_writelane_b32 v254, s8, 43
	s_or_b32 s2, s8, 1
	v_writelane_b32 v254, s2, 44
	s_add_u32 s2, s16, 0x100c00
	s_addc_u32 s3, s17, 0
	v_writelane_b32 v254, s2, 45
	s_ashr_i32 s89, s88, 31
	s_nop 0
	v_writelane_b32 v254, s3, 46
	v_readlane_b32 s2, v251, 29
	v_readlane_b32 s3, v251, 30
	s_ashr_i32 s3, s2, 31
	v_writelane_b32 v251, s2, 29
	s_nop 1
	v_writelane_b32 v251, s3, 30
	s_mov_b32 s2, 1
	v_writelane_b32 v254, s2, 47
	s_add_i32 s2, 0, 0x19a00
	v_writelane_b32 v254, s2, 48
	s_add_i32 s2, 0, 0x13200
	v_writelane_b32 v254, s2, 49
	s_add_i32 s2, 0, 0x17600
	v_writelane_b32 v254, s2, 50
	s_add_i32 s2, 0, 0x20080
	v_writelane_b32 v254, s2, 51
	s_add_i32 s2, 0, 0x20120
	v_writelane_b32 v254, s2, 52
	s_add_i32 s2, 0, 0x201c0
	v_writelane_b32 v254, s2, 53
	v_cmp_eq_u32_e64 s[2:3], 0, v0
	s_nop 1
	v_writelane_b32 v254, s2, 54
	s_nop 1
	v_writelane_b32 v254, s3, 55
	s_lshl_b64 s[2:3], s[88:89], 12
	v_writelane_b32 v254, s2, 56
	s_nop 1
	v_writelane_b32 v254, s3, 57
	s_lshl_b64 s[2:3], s[88:89], 13
	v_writelane_b32 v254, s2, 58
	s_nop 1
	v_writelane_b32 v254, s3, 59
	s_mov_b64 s[2:3], s[16:17]
	v_writelane_b32 v254, s2, 60
	s_nop 1
	v_writelane_b32 v254, s3, 61
	v_writelane_b32 v254, s66, 62
	s_mov_b32 s2, s88
	v_writelane_b32 v254, s2, 63
	s_nop 1
	v_writelane_b32 v250, s3, 0
	v_writelane_b32 v250, s78, 1
	s_nop 1
	v_writelane_b32 v250, s79, 2
	v_writelane_b32 v250, s96, 3
	s_nop 1
	v_writelane_b32 v250, s97, 4
	v_writelane_b32 v250, s26, 5
	s_nop 1
	v_writelane_b32 v250, s27, 6
	s_branch .LBB0_106

.LBB0_387:
	v_lshlrev_b32_e32 v2, 3, v38
	s_mulk_i32 s5, 0x2100
	v_lshrrev_b32_e32 v40, 3, v38
	v_and_b32_e32 v2, 56, v2
	s_add_i32 s5, s5, 0
	v_lshrrev_b32_e32 v37, 5, v38
	v_and_b32_e32 v36, 31, v1
	v_mul_u32_u24_e32 v38, 0x84, v2
	v_lshlrev_b32_e32 v41, 2, v40
	v_lshl_add_u32 v39, v36, 2, s5
	v_mul_u32_u24_e32 v45, 0x84, v37
	v_add3_u32 v41, s5, v38, v41
	s_lshl_b32 s5, s33, 6
	v_or_b32_e32 v42, 8, v40
	v_or_b32_e32 v43, 16, v40
	v_or_b32_e32 v44, 24, v40
	s_lshl_b32 s52, s33, 5
	s_add_i32 s53, s5, 0x23800
	v_lshlrev_b32_e32 v38, 1, v2
	v_add_u32_e32 v45, v39, v45
	s_branch .LBB0_389
.LBB0_388:
	s_add_i32 s52, s52, 0x11c00
	s_add_i32 s53, s53, 0x23800
	s_andn2_b64 vcc, exec, s[40:41]
	s_mov_b32 s33, s5
	s_cbranch_vccz .LBB0_443
.LBB0_389:
	s_cmp_lt_i32 s33, 0x36d90
	s_cselect_b64 s[38:39], -1, 0
	s_cmp_gt_i32 s33, 0x36d8f
	s_cbranch_scc1 .LBB0_414
	s_add_i32 s5, s33, 0x470
	s_cmpk_gt_i32 s33, 0x3b8f
	s_mov_b64 s[48:49], -1
	s_cbranch_scc0 .LBB0_411
	s_cmpk_gt_u32 s5, 0x4fff
	s_cbranch_scc0 .LBB0_408
	s_cmpk_gt_u32 s5, 0x51ff
	s_cbranch_scc0 .LBB0_405
	s_cmpk_gt_u32 s5, 0x61ff
	s_cbranch_scc0 .LBB0_402
	s_cmpk_gt_u32 s5, 0x71ff
	s_cbranch_scc0 .LBB0_399
	s_cmp_gt_u32 s5, 0x271ff
	s_mov_b64 s[14:15], -1
	s_cbranch_scc0 .LBB0_397
	s_add_i32 s9, s33, 0xfffd9270
	s_lshr_b32 s34, s9, 9
	s_bfe_u32 s10, s5, 0x30006
	s_lshl_b64 s[12:13], s[34:35], 22
	v_readlane_b32 s56, v251, 0
	v_readlane_b32 s57, v251, 1
	s_add_u32 s40, s56, s12
	s_addc_u32 s41, s57, s13
	s_lshl_b64 s[12:13], s[34:35], 21
	v_readlane_b32 s9, v253, 36
	s_add_u32 s12, s9, s12
	v_readlane_b32 s9, v253, 37
	s_addc_u32 s13, s9, s13
	s_add_i32 s9, s52, 0x8e00
	v_readlane_b32 s58, v251, 2
	v_readlane_b32 s59, v251, 3
	v_readlane_b32 s60, v251, 4
	v_readlane_b32 s61, v251, 5
	v_readlane_b32 s62, v251, 6
	v_readlane_b32 s63, v251, 7
	s_and_b32 s54, s9, 0x7e0
	s_mov_b64 s[14:15], 0
.LBB0_397:
	s_andn2_b64 vcc, exec, s[14:15]
	s_cbranch_vccnz .LBB0_441
	s_cmp_gt_u32 s5, 0x171ff
	s_cselect_b64 s[12:13], -1, 0
	s_and_b64 s[10:11], s[12:13], exec
	s_mov_b32 s10, 0xfffe8e00
	s_cselect_b32 s9, 0x80, 0
	s_cselect_b32 s10, s10, 0xffff8e00
	s_add_i32 s11, s52, 0x8e00
	s_add_i32 s14, s53, 0xfffee400
	s_add_i32 s10, s10, s33
	s_and_b32 s14, s14, 0x300
	s_and_b32 s15, s11, 0x60
	s_addk_i32 s10, 0x470
	s_or_b32 s14, s14, s15
	s_lshr_b32 s34, s10, 9
	s_bfe_u32 s10, s5, 0x50004
	s_or_b32 s54, s14, s9
	v_readlane_b32 s68, v251, 31
	s_and_b64 s[12:13], s[12:13], exec
	v_readlane_b32 s80, v251, 43
	v_readlane_b32 s81, v251, 44
	v_readlane_b32 s82, v251, 45
	v_readlane_b32 s83, v251, 46
	s_cselect_b32 s9, s83, s81
	s_cselect_b32 s14, s82, s80
	s_lshl_b64 s[12:13], s[34:35], 22
	s_add_u32 s40, s14, s12
	v_readlane_b32 s78, v251, 41
	v_readlane_b32 s79, v251, 42
	s_addc_u32 s41, s9, s13
	v_readlane_b32 s9, v253, 34
	v_readlane_b32 s78, v250, 1
	s_add_u32 s12, s9, s12
	v_readlane_b32 s9, v253, 35
	v_readlane_b32 s69, v251, 32
	v_readlane_b32 s70, v251, 33
	v_readlane_b32 s71, v251, 34
	v_readlane_b32 s72, v251, 35
	v_readlane_b32 s73, v251, 36
	v_readlane_b32 s74, v251, 37
	v_readlane_b32 s75, v251, 38
	v_readlane_b32 s76, v251, 39
	v_readlane_b32 s77, v251, 40
	v_readlane_b32 s79, v250, 2
	s_addc_u32 s13, s9, s13
	s_and_b32 s44, s11, 0x1e0
	s_mov_b64 s[42:43], 0x200
	s_movk_i32 s14, 0x800
	s_mov_b64 s[48:49], 0

.LBB0_400:
	s_add_i32 s9, s33, 0xffffa270
	s_and_b32 s34, s9, 0xfffff800
	s_bfe_u32 s10, s9, 0x50006
	s_lshl_b64 s[12:13], s[34:35], 13
	v_readlane_b32 s68, v251, 31
	v_readlane_b32 s69, v251, 32
	s_add_u32 s40, s68, s12
	s_addc_u32 s41, s69, s13
	s_lshl_b64 s[12:13], s[34:35], 12
	v_readlane_b32 s9, v253, 22
	s_add_u32 s12, s9, s12
	v_readlane_b32 s9, v253, 23
	v_readlane_b32 s78, v251, 41
	v_readlane_b32 s79, v251, 42
	s_addc_u32 s13, s9, s13
	s_add_i32 s9, s52, 0x8e00
	v_readlane_b32 s78, v250, 1
	s_and_b32 s54, s9, 0x7e0
	v_readlane_b32 s79, v250, 2
	s_mov_b64 s[42:43], 0x800
	s_movk_i32 s14, 0x800
	s_mov_b32 s44, s54
	v_readlane_b32 s70, v251, 33
	v_readlane_b32 s71, v251, 34
	v_readlane_b32 s72, v251, 35
	v_readlane_b32 s73, v251, 36
	v_readlane_b32 s74, v251, 37
	v_readlane_b32 s75, v251, 38
	v_readlane_b32 s76, v251, 39
	v_readlane_b32 s77, v251, 40
	v_readlane_b32 s80, v251, 43
	v_readlane_b32 s81, v251, 44
	v_readlane_b32 s82, v251, 45
	v_readlane_b32 s83, v251, 46

.LBB0_402:
	s_andn2_b64 vcc, exec, s[48:49]
	s_cbranch_vccnz .LBB0_404
	s_add_i32 s9, s33, 0xffffb270
	s_and_b32 s34, s9, 0xfffff800
	v_readlane_b32 s68, v251, 12
	s_bfe_u32 s10, s9, 0x50006
	s_lshl_b64 s[12:13], s[34:35], 13
	v_readlane_b32 s80, v251, 24
	v_readlane_b32 s81, v251, 25
	s_add_u32 s40, s80, s12
	s_addc_u32 s41, s81, s13
	s_lshl_b64 s[12:13], s[34:35], 12
	v_readlane_b32 s9, v252, 1
	s_add_u32 s12, s9, s12
	v_readlane_b32 s9, v252, 2
	v_readlane_b32 s78, v251, 22
	v_readlane_b32 s79, v251, 23
	s_addc_u32 s13, s9, s13
	s_add_i32 s9, s52, 0x8e00
	v_readlane_b32 s78, v250, 1
	s_and_b32 s54, s9, 0x7e0
	v_readlane_b32 s79, v250, 2
	s_mov_b64 s[42:43], 0x800
	s_movk_i32 s14, 0x800
	s_mov_b32 s44, s54
	v_readlane_b32 s69, v251, 13
	v_readlane_b32 s70, v251, 14
	v_readlane_b32 s71, v251, 15
	v_readlane_b32 s72, v251, 16
	v_readlane_b32 s73, v251, 17
	v_readlane_b32 s74, v251, 18
	v_readlane_b32 s75, v251, 19
	v_readlane_b32 s76, v251, 20
	v_readlane_b32 s77, v251, 21
	v_readlane_b32 s82, v251, 26
	v_readlane_b32 s83, v251, 27

.LBB0_406:
	s_add_i32 s9, s33, 0xffffb470
	s_lshr_b32 s10, s9, 4
	s_add_i32 s9, s52, 0x8e00
	s_and_b32 s54, s9, 0x1e0
	s_mov_b64 s[42:43], 0x200
	s_movk_i32 s14, 0x800
	s_mov_b64 s[12:13], s[26:27]
	s_mov_b32 s44, s54

.LBB0_408:
	s_andn2_b64 vcc, exec, s[48:49]
	s_cbranch_vccnz .LBB0_410
	s_and_b32 s9, s5, 0x7800
	s_add_i32 s34, s9, 0xffffc000
	v_readlane_b32 s68, v251, 12
	s_bfe_u32 s10, s5, 0x50006
	s_lshl_b64 s[12:13], s[34:35], 13
	v_readlane_b32 s76, v251, 20
	v_readlane_b32 s77, v251, 21
	s_add_u32 s40, s76, s12
	s_addc_u32 s41, s77, s13
	s_lshl_b64 s[12:13], s[34:35], 12
	v_readlane_b32 s9, v253, 32
	s_add_u32 s12, s9, s12
	v_readlane_b32 s9, v253, 33
	v_readlane_b32 s78, v251, 22
	v_readlane_b32 s79, v251, 23
	s_addc_u32 s13, s9, s13
	s_add_i32 s9, s52, 0x8e00
	v_readlane_b32 s78, v250, 1
	s_and_b32 s54, s9, 0x7e0
	v_readlane_b32 s79, v250, 2
	s_mov_b64 s[42:43], 0x800
	s_movk_i32 s14, 0x800
	s_mov_b32 s44, s54
	v_readlane_b32 s69, v251, 13
	v_readlane_b32 s70, v251, 14
	v_readlane_b32 s71, v251, 15
	v_readlane_b32 s72, v251, 16
	v_readlane_b32 s73, v251, 17
	v_readlane_b32 s74, v251, 18
	v_readlane_b32 s75, v251, 19
	v_readlane_b32 s80, v251, 24
	v_readlane_b32 s81, v251, 25
	v_readlane_b32 s82, v251, 26
	v_readlane_b32 s83, v251, 27

.LBB0_414:
	v_add_u32_e32 v78, 0x400, v45
	v_add_u32_e32 v79, 0x800, v45
	v_add_u32_e32 v80, 0xc00, v45
	v_add_u32_e32 v81, 0x1000, v45
	v_add_u32_e32 v82, 0x1400, v45
	v_add_u32_e32 v83, 0x1800, v45
	v_add_u32_e32 v88, 0x1c00, v45
	s_waitcnt vmcnt(0)
	ds_write2_b32 v45, v4, v5 offset1:66
	ds_write2_b32 v45, v6, v7 offset0:132 offset1:198
	ds_write2_b32 v78, v8, v9 offset0:8 offset1:74
	ds_write2_b32 v78, v10, v11 offset0:140 offset1:206
	ds_write2_b32 v79, v12, v13 offset0:16 offset1:82
	ds_write2_b32 v79, v14, v15 offset0:148 offset1:214
	ds_write2_b32 v80, v16, v17 offset0:24 offset1:90
	ds_write2_b32 v80, v18, v19 offset0:156 offset1:222
	ds_write2_b32 v81, v20, v21 offset0:32 offset1:98
	ds_write2_b32 v81, v22, v23 offset0:164 offset1:230
	ds_write2_b32 v82, v24, v25 offset0:40 offset1:106
	ds_write2_b32 v82, v26, v27 offset0:172 offset1:238
	ds_write2_b32 v83, v28, v29 offset0:48 offset1:114
	ds_write2_b32 v83, v30, v31 offset0:180 offset1:246
	ds_write2_b32 v88, v32, v33 offset0:56 offset1:122
	ds_write2_b32 v88, v34, v35 offset0:188 offset1:254
	v_add_u32_e32 v2, s47, v40
	s_waitcnt lgkmcnt(0)
	v_ashrrev_i32_e32 v39, 8, v2
	s_ashr_i32 s9, s8, 31
	ds_read2_b32 v[94:95], v41 offset0:33 offset1:41
	ds_read2_b32 v[96:97], v41 offset1:8
	ds_read2_b32 v[98:99], v41 offset0:66 offset1:74
	ds_read2_b32 v[100:101], v41 offset0:99 offset1:107
	ds_read2_b32 v[102:103], v41 offset0:132 offset1:140
	ds_read2_b32 v[104:105], v41 offset0:165 offset1:173
	ds_read2_b32 v[106:107], v41 offset0:198 offset1:206
	ds_read2_b32 v[108:109], v41 offset0:231 offset1:239
	v_ashrrev_i32_e32 v89, 31, v39
	s_lshl_b32 s11, s8, 8
	s_lshr_b64 s[40:41], s[8:9], 24
	s_waitcnt lgkmcnt(0)
	v_cvt_pk_bf16_f32 v90, v96, v94
	v_mul_lo_u32 v94, s40, v39
	v_mul_lo_u32 v89, s11, v89
	v_mad_u64_u32 v[110:111], s[42:43], s11, v39, 0
	v_add3_u32 v111, v111, v89, v94
	s_ashr_i32 s5, s4, 31
	v_lshl_add_u64 v[110:111], v[110:111], 1, s[6:7]
	s_lshl_b64 s[42:43], s[4:5], 15
	v_lshlrev_b32_e32 v2, 7, v2
	v_lshl_add_u64 v[110:111], v[110:111], 0, s[42:43]
	v_and_b32_e32 v2, 0x7f80, v2
	v_lshl_add_u64 v[110:111], v[110:111], 0, v[2:3]
	v_add_u32_e32 v2, s47, v42
	v_mov_b32_e32 v39, v3
	v_ashrrev_i32_e32 v89, 8, v2
	v_cvt_pk_bf16_f32 v91, v98, v100
	v_cvt_pk_bf16_f32 v92, v102, v104
	v_cvt_pk_bf16_f32 v93, v106, v108
	v_lshl_add_u64 v[110:111], v[110:111], 0, v[38:39]
	v_ashrrev_i32_e32 v94, 31, v89
	global_store_dwordx4 v[110:111], v[90:93], off nt
	v_mul_lo_u32 v96, s40, v89
	v_lshlrev_b32_e32 v2, 7, v2
	v_cvt_pk_bf16_f32 v90, v97, v95
	v_mul_lo_u32 v97, s11, v94
	v_mad_u64_u32 v[94:95], s[44:45], s11, v89, 0
	v_add3_u32 v95, v95, v97, v96
	v_lshl_add_u64 v[94:95], v[94:95], 1, s[6:7]
	v_lshl_add_u64 v[94:95], v[94:95], 0, s[42:43]
	v_and_b32_e32 v2, 0x7f80, v2
	v_lshl_add_u64 v[94:95], v[94:95], 0, v[2:3]
	v_add_u32_e32 v2, s47, v43
	v_cvt_pk_bf16_f32 v91, v99, v101
	v_cvt_pk_bf16_f32 v92, v103, v105
	v_cvt_pk_bf16_f32 v93, v107, v109
	v_lshl_add_u64 v[94:95], v[94:95], 0, v[38:39]
	v_ashrrev_i32_e32 v89, 8, v2
	ds_read2_b32 v[96:97], v41 offset0:16 offset1:24
	ds_read2_b32 v[98:99], v41 offset0:49 offset1:57
	ds_read2_b32 v[100:101], v41 offset0:82 offset1:90
	ds_read2_b32 v[102:103], v41 offset0:115 offset1:123
	ds_read2_b32 v[104:105], v41 offset0:148 offset1:156
	ds_read2_b32 v[106:107], v41 offset0:181 offset1:189
	ds_read2_b32 v[108:109], v41 offset0:214 offset1:222
	ds_read2_b32 v[110:111], v41 offset0:247 offset1:255
	global_store_dwordx4 v[94:95], v[90:93], off nt
	v_ashrrev_i32_e32 v94, 31, v89
	v_lshlrev_b32_e32 v2, 7, v2
	s_waitcnt lgkmcnt(6)
	v_cvt_pk_bf16_f32 v90, v96, v98
	v_mul_lo_u32 v96, s40, v89
	v_mul_lo_u32 v98, s11, v94
	v_mad_u64_u32 v[94:95], s[44:45], s11, v89, 0
	v_add3_u32 v95, v95, v98, v96
	v_lshl_add_u64 v[94:95], v[94:95], 1, s[6:7]
	v_lshl_add_u64 v[94:95], v[94:95], 0, s[42:43]
	v_and_b32_e32 v2, 0x7f80, v2
	v_lshl_add_u64 v[94:95], v[94:95], 0, v[2:3]
	v_add_u32_e32 v2, s47, v44
	s_waitcnt lgkmcnt(4)
	v_cvt_pk_bf16_f32 v91, v100, v102
	s_waitcnt lgkmcnt(2)
	v_cvt_pk_bf16_f32 v92, v104, v106
	s_waitcnt lgkmcnt(0)
	v_cvt_pk_bf16_f32 v93, v108, v110
	v_lshl_add_u64 v[94:95], v[94:95], 0, v[38:39]
	v_ashrrev_i32_e32 v89, 8, v2
	global_store_dwordx4 v[94:95], v[90:93], off nt
	v_ashrrev_i32_e32 v94, 31, v89
	v_mul_lo_u32 v96, s40, v89
	v_cvt_pk_bf16_f32 v90, v97, v99
	v_mul_lo_u32 v97, s11, v94
	v_mad_u64_u32 v[94:95], s[40:41], s11, v89, 0
	v_add3_u32 v95, v95, v97, v96
	v_lshl_add_u64 v[94:95], v[94:95], 1, s[6:7]
	v_lshlrev_b32_e32 v2, 7, v2
	v_lshl_add_u64 v[94:95], v[94:95], 0, s[42:43]
	v_and_b32_e32 v2, 0x7f80, v2
	v_lshl_add_u64 v[94:95], v[94:95], 0, v[2:3]
	v_cvt_pk_bf16_f32 v91, v101, v103
	v_cvt_pk_bf16_f32 v92, v105, v107
	v_cvt_pk_bf16_f32 v93, v109, v111
	v_lshl_add_u64 v[94:95], v[94:95], 0, v[38:39]
	global_store_dwordx4 v[94:95], v[90:93], off nt
	s_add_i32 s5, s33, 0x8e0
	s_waitcnt lgkmcnt(0)
	s_cmp_gt_i32 s33, 0x3691f
	s_cselect_b64 s[40:41], -1, 0
	s_and_b64 vcc, exec, s[40:41]
	s_cbranch_vccnz .LBB0_439
	s_cmpk_gt_i32 s33, 0x371f
	s_mov_b64 s[50:51], -1
	s_cbranch_scc0 .LBB0_436
	s_cmpk_gt_u32 s5, 0x4fff
	s_cbranch_scc0 .LBB0_433
	s_cmpk_gt_u32 s5, 0x51ff
	s_cbranch_scc0 .LBB0_430
	s_cmpk_gt_u32 s5, 0x61ff
	s_cbranch_scc0 .LBB0_427
	s_cmpk_gt_u32 s5, 0x71ff
	s_cbranch_scc0 .LBB0_424
	s_cmp_gt_u32 s5, 0x271ff
	s_mov_b64 s[8:9], -1
	s_cbranch_scc0 .LBB0_422
	s_add_i32 s4, s33, 0xfffd96e0
	s_lshr_b32 s34, s4, 9
	s_bfe_u32 s4, s5, 0x30006
	s_lshl_b64 s[6:7], s[34:35], 22
	v_readlane_b32 s56, v251, 0
	v_readlane_b32 s57, v251, 1
	s_add_u32 s42, s56, s6
	s_addc_u32 s43, s57, s7
	s_lshl_b64 s[6:7], s[34:35], 21
	v_readlane_b32 s8, v253, 36
	s_add_u32 s6, s8, s6
	v_readlane_b32 s8, v253, 37
	s_addc_u32 s7, s8, s7
	s_add_i32 s8, s52, 0x11c00
	v_readlane_b32 s58, v251, 2
	v_readlane_b32 s59, v251, 3
	v_readlane_b32 s60, v251, 4
	v_readlane_b32 s61, v251, 5
	v_readlane_b32 s62, v251, 6
	v_readlane_b32 s63, v251, 7
	s_and_b32 s47, s8, 0x7e0
	s_mov_b64 s[8:9], 0
.LBB0_422:
	s_andn2_b64 vcc, exec, s[8:9]
	s_cbranch_vccnz .LBB0_442
	s_cmp_gt_u32 s5, 0x171ff
	s_cselect_b64 s[6:7], -1, 0
	s_and_b64 s[8:9], s[6:7], exec
	s_mov_b32 s4, 0xfffe8e00
	s_cselect_b32 s8, 0x80, 0
	s_cselect_b32 s4, s4, 0xffff8e00
	s_add_i32 s9, s52, 0x11c00
	s_add_i32 s4, s4, s33
	s_and_b32 s11, s53, 0x300
	s_and_b32 s9, s9, 0x60
	s_addk_i32 s4, 0x8e0
	s_or_b32 s9, s11, s9
	s_lshr_b32 s34, s4, 9
	s_bfe_u32 s4, s5, 0x50004
	s_or_b32 s47, s9, s8
	v_readlane_b32 s68, v251, 31
	s_and_b64 s[6:7], s[6:7], exec
	v_readlane_b32 s80, v251, 43
	v_readlane_b32 s81, v251, 44
	v_readlane_b32 s82, v251, 45
	v_readlane_b32 s83, v251, 46
	s_cselect_b32 s8, s83, s81
	s_cselect_b32 s9, s82, s80
	s_lshl_b64 s[6:7], s[34:35], 22
	s_add_u32 s42, s9, s6
	v_readlane_b32 s78, v251, 41
	v_readlane_b32 s79, v251, 42
	s_addc_u32 s43, s8, s7
	v_readlane_b32 s8, v253, 34
	v_readlane_b32 s78, v250, 1
	s_add_u32 s6, s8, s6
	v_readlane_b32 s8, v253, 35
	v_readlane_b32 s69, v251, 32
	v_readlane_b32 s70, v251, 33
	v_readlane_b32 s71, v251, 34
	v_readlane_b32 s72, v251, 35
	v_readlane_b32 s73, v251, 36
	v_readlane_b32 s74, v251, 37
	v_readlane_b32 s75, v251, 38
	v_readlane_b32 s76, v251, 39
	v_readlane_b32 s77, v251, 40
	v_readlane_b32 s79, v250, 2
	s_addc_u32 s7, s8, s7
	s_and_b32 s48, s52, 0x1e0
	s_mov_b64 s[44:45], 0x200
	s_movk_i32 s8, 0x800
	s_mov_b64 s[50:51], 0

.LBB0_425:
	s_add_i32 s4, s33, 0xffffa6e0
	s_and_b32 s34, s4, 0xfffff800
	s_bfe_u32 s4, s4, 0x50006
	s_lshl_b64 s[6:7], s[34:35], 13
	v_readlane_b32 s68, v251, 31
	v_readlane_b32 s69, v251, 32
	s_add_u32 s42, s68, s6
	s_addc_u32 s43, s69, s7
	s_lshl_b64 s[6:7], s[34:35], 12
	v_readlane_b32 s8, v253, 22
	s_add_u32 s6, s8, s6
	v_readlane_b32 s8, v253, 23
	v_readlane_b32 s78, v251, 41
	v_readlane_b32 s79, v251, 42
	s_addc_u32 s7, s8, s7
	s_add_i32 s8, s52, 0x11c00
	v_readlane_b32 s78, v250, 1
	s_and_b32 s47, s8, 0x7e0
	v_readlane_b32 s79, v250, 2
	s_mov_b64 s[44:45], 0x800
	s_movk_i32 s8, 0x800
	s_mov_b32 s48, s47
	v_readlane_b32 s70, v251, 33
	v_readlane_b32 s71, v251, 34
	v_readlane_b32 s72, v251, 35
	v_readlane_b32 s73, v251, 36
	v_readlane_b32 s74, v251, 37
	v_readlane_b32 s75, v251, 38
	v_readlane_b32 s76, v251, 39
	v_readlane_b32 s77, v251, 40
	v_readlane_b32 s80, v251, 43
	v_readlane_b32 s81, v251, 44
	v_readlane_b32 s82, v251, 45
	v_readlane_b32 s83, v251, 46

.LBB0_427:
	s_andn2_b64 vcc, exec, s[50:51]
	s_cbranch_vccnz .LBB0_429
	s_add_i32 s4, s33, 0xffffb6e0
	s_and_b32 s34, s4, 0xfffff800
	v_readlane_b32 s68, v251, 12
	s_bfe_u32 s4, s4, 0x50006
	s_lshl_b64 s[6:7], s[34:35], 13
	v_readlane_b32 s80, v251, 24
	v_readlane_b32 s81, v251, 25
	s_add_u32 s42, s80, s6
	s_addc_u32 s43, s81, s7
	s_lshl_b64 s[6:7], s[34:35], 12
	v_readlane_b32 s8, v252, 1
	s_add_u32 s6, s8, s6
	v_readlane_b32 s8, v252, 2
	v_readlane_b32 s78, v251, 22
	v_readlane_b32 s79, v251, 23
	s_addc_u32 s7, s8, s7
	s_add_i32 s8, s52, 0x11c00
	v_readlane_b32 s78, v250, 1
	s_and_b32 s47, s8, 0x7e0
	v_readlane_b32 s79, v250, 2
	s_mov_b64 s[44:45], 0x800
	s_movk_i32 s8, 0x800
	s_mov_b32 s48, s47
	v_readlane_b32 s69, v251, 13
	v_readlane_b32 s70, v251, 14
	v_readlane_b32 s71, v251, 15
	v_readlane_b32 s72, v251, 16
	v_readlane_b32 s73, v251, 17
	v_readlane_b32 s74, v251, 18
	v_readlane_b32 s75, v251, 19
	v_readlane_b32 s76, v251, 20
	v_readlane_b32 s77, v251, 21
	v_readlane_b32 s82, v251, 26
	v_readlane_b32 s83, v251, 27

.LBB0_431:
	s_add_i32 s4, s33, 0xffffb8e0
	s_and_b32 s47, s52, 0x1e0
	s_lshr_b32 s4, s4, 4
	s_mov_b64 s[44:45], 0x200
	s_movk_i32 s8, 0x800
	s_mov_b64 s[6:7], s[26:27]
	s_mov_b32 s48, s47

.LBB0_433:
	s_andn2_b64 vcc, exec, s[50:51]
	s_cbranch_vccnz .LBB0_435
	s_and_b32 s4, s5, 0x7800
	s_add_i32 s34, s4, 0xffffc000
	v_readlane_b32 s68, v251, 12
	s_bfe_u32 s4, s5, 0x50006
	s_lshl_b64 s[6:7], s[34:35], 13
	v_readlane_b32 s76, v251, 20
	v_readlane_b32 s77, v251, 21
	s_add_u32 s42, s76, s6
	s_addc_u32 s43, s77, s7
	s_lshl_b64 s[6:7], s[34:35], 12
	v_readlane_b32 s8, v253, 32
	s_add_u32 s6, s8, s6
	v_readlane_b32 s8, v253, 33
	v_readlane_b32 s78, v251, 22
	v_readlane_b32 s79, v251, 23
	s_addc_u32 s7, s8, s7
	s_add_i32 s8, s52, 0x11c00
	v_readlane_b32 s78, v250, 1
	s_and_b32 s47, s8, 0x7e0
	v_readlane_b32 s79, v250, 2
	s_mov_b64 s[44:45], 0x800
	s_movk_i32 s8, 0x800
	s_mov_b32 s48, s47
	v_readlane_b32 s69, v251, 13
	v_readlane_b32 s70, v251, 14
	v_readlane_b32 s71, v251, 15
	v_readlane_b32 s72, v251, 16
	v_readlane_b32 s73, v251, 17
	v_readlane_b32 s74, v251, 18
	v_readlane_b32 s75, v251, 19
	v_readlane_b32 s80, v251, 24
	v_readlane_b32 s81, v251, 25
	v_readlane_b32 s82, v251, 26
	v_readlane_b32 s83, v251, 27

.LBB0_436:
	s_andn2_b64 vcc, exec, s[50:51]
	s_cbranch_vccnz .LBB0_438
	s_ashr_i32 s4, s5, 31
	s_lshr_b32 s4, s4, 19
	s_add_i32 s4, s5, s4
	s_ashr_i32 s6, s4, 13
	s_and_b32 s4, s4, 0xe000
	s_sub_i32 s4, s33, s4
	s_add_i32 s7, s4, 0x8e0
	s_sext_i32_i16 s4, s7
	s_bfe_u32 s4, s4, 0x80017
	s_add_i32 s8, s7, s4
	s_sext_i32_i16 s4, s8
	s_and_b32 s8, s8, 0xff00
	s_sub_i32 s7, s7, s8
	s_sext_i32_i16 s11, s7
	s_ashr_i32 s7, s6, 31
	v_readlane_b32 s68, v251, 12
	s_ashr_i32 s4, s4, 8
	s_lshl_b64 s[8:9], s[6:7], 26
	v_readlane_b32 s70, v251, 14
	v_readlane_b32 s71, v251, 15
	s_add_u32 s42, s70, s8
	s_addc_u32 s43, s71, s9
	s_lshl_b64 s[6:7], s[6:7], 25
	v_readlane_b32 s8, v253, 30
	v_readlane_b32 s78, v251, 22
	v_readlane_b32 s79, v251, 23
	s_add_u32 s6, s8, s6
	v_readlane_b32 s8, v253, 31
	v_readlane_b32 s78, v250, 1
	s_addc_u32 s7, s8, s7
	s_lshl_b32 s48, s11, 5
	v_readlane_b32 s79, v250, 2
	s_movk_i32 s8, 0x800
	s_mov_b64 s[44:45], 0x2000
	s_mov_b32 s47, s48
	v_readlane_b32 s69, v251, 13
	v_readlane_b32 s72, v251, 16
	v_readlane_b32 s73, v251, 17
	v_readlane_b32 s74, v251, 18
	v_readlane_b32 s75, v251, 19
	v_readlane_b32 s76, v251, 20
	v_readlane_b32 s77, v251, 21
	v_readlane_b32 s80, v251, 24
	v_readlane_b32 s81, v251, 25
	v_readlane_b32 s82, v251, 26
	v_readlane_b32 s83, v251, 27

.LBB0_445:
	s_or_b64 exec, exec, s[8:9]
	s_mov_b32 s8, 0x38fff
	v_cmp_lt_i32_e32 vcc, s8, v1
	v_add_u32_e32 v28, 0x11c000, v28
	s_or_b64 s[6:7], vcc, s[6:7]
	v_add_u32_e32 v1, 0x47000, v1
	s_andn2_b64 exec, exec, s[6:7]
	s_cbranch_execz .LBB0_482

.LBB0_452:
	s_or_b64 exec, exec, s[8:9]
	v_add_u32_e32 v9, 0x11c00, v1
	v_ashrrev_i32_e32 v11, 31, v9
	v_lshrrev_b32_e32 v10, 15, v11
	v_lshrrev_b32_e32 v11, 21, v11
	v_add_u32_e32 v11, v9, v11
	v_ashrrev_i32_e32 v11, 11, v11
	v_lshrrev_b32_e32 v12, 26, v11
	v_add_u32_e32 v12, v11, v12
	v_and_b32_e32 v12, 0xffffffc0, v12
	v_add_u32_e32 v10, v9, v10
	v_sub_u32_e32 v12, v11, v12
	v_mul_i32_i24_e32 v11, 0x800, v11
	s_mov_b32 s8, 0x6e400
	v_ashrrev_i32_e32 v10, 17, v10
	v_sub_u32_e32 v14, v9, v11
	v_cmp_gt_i32_e32 vcc, s8, v1
	v_mov_b32_e32 v9, 0
	v_mov_b32_e32 v13, 0
	s_and_saveexec_b64 s[8:9], vcc
	s_cbranch_execz .LBB0_460
	v_cmp_lt_i32_e32 vcc, 3, v12
	s_and_saveexec_b64 s[10:11], vcc
	s_xor_b64 s[10:11], exec, s[10:11]
	s_cbranch_execz .LBB0_457
	v_cmp_gt_u32_e32 vcc, 36, v12
	v_mov_b32_e32 v13, 0
	s_and_saveexec_b64 s[12:13], vcc
	s_cbranch_execz .LBB0_456
	v_ashrrev_i32_e32 v11, 31, v10
	v_readlane_b32 s48, v251, 31
	v_ashrrev_i32_e32 v15, 31, v14
	v_lshlrev_b64 v[16:17], 18, v[10:11]
	v_readlane_b32 s56, v251, 39
	v_readlane_b32 s57, v251, 40
	v_lshlrev_b64 v[18:19], 7, v[14:15]
	v_mov_b32_e32 v13, v3
	v_lshl_add_u64 v[16:17], s[56:57], 0, v[16:17]
	v_lshl_add_u64 v[16:17], v[16:17], 0, v[18:19]
	v_lshl_add_u64 v[16:17], v[12:13], 2, v[16:17]
	global_load_dword v13, v[16:17], off offset:-16
	v_readlane_b32 s49, v251, 32
	v_readlane_b32 s50, v251, 33
	v_readlane_b32 s51, v251, 34
	v_readlane_b32 s52, v251, 35
	v_readlane_b32 s53, v251, 36
	v_readlane_b32 s54, v251, 37
	v_readlane_b32 s55, v251, 38
	v_readlane_b32 s58, v251, 41
	v_readlane_b32 s59, v251, 42
	v_readlane_b32 s60, v251, 43
	v_readlane_b32 s61, v251, 44
	v_readlane_b32 s62, v251, 45
	v_readlane_b32 s63, v251, 46

.LBB0_460:
	s_or_b64 exec, exec, s[8:9]
	v_add_u32_e32 v11, 0x23800, v1
	v_ashrrev_i32_e32 v15, 31, v11
	v_lshrrev_b32_e32 v16, 15, v15
	v_lshrrev_b32_e32 v15, 21, v15
	v_add_u32_e32 v15, v11, v15
	v_ashrrev_i32_e32 v15, 11, v15
	v_lshrrev_b32_e32 v17, 26, v15
	v_add_u32_e32 v17, v15, v17
	v_and_b32_e32 v17, 0xffffffc0, v17
	v_add_u32_e32 v16, v11, v16
	v_sub_u32_e32 v18, v15, v17
	v_mul_i32_i24_e32 v15, 0x800, v15
	s_mov_b32 s8, 0x5c800
	v_ashrrev_i32_e32 v16, 17, v16
	v_sub_u32_e32 v20, v11, v15
	v_cmp_gt_i32_e32 vcc, s8, v1
	s_and_saveexec_b64 s[8:9], vcc
	s_cbranch_execz .LBB0_468
	v_cmp_lt_i32_e32 vcc, 3, v18
	s_and_saveexec_b64 s[10:11], vcc
	s_xor_b64 s[10:11], exec, s[10:11]
	s_cbranch_execz .LBB0_465
	v_cmp_gt_u32_e32 vcc, 36, v18
	v_mov_b32_e32 v9, 0
	s_and_saveexec_b64 s[12:13], vcc
	s_cbranch_execz .LBB0_464
	v_ashrrev_i32_e32 v17, 31, v16
	v_readlane_b32 s48, v251, 31
	v_ashrrev_i32_e32 v21, 31, v20
	v_lshlrev_b64 v[22:23], 18, v[16:17]
	v_readlane_b32 s56, v251, 39
	v_readlane_b32 s57, v251, 40
	v_lshlrev_b64 v[24:25], 7, v[20:21]
	v_mov_b32_e32 v19, v3
	v_lshl_add_u64 v[22:23], s[56:57], 0, v[22:23]
	v_lshl_add_u64 v[22:23], v[22:23], 0, v[24:25]
	v_lshl_add_u64 v[22:23], v[18:19], 2, v[22:23]
	global_load_dword v9, v[22:23], off offset:-16
	v_readlane_b32 s49, v251, 32
	v_readlane_b32 s50, v251, 33
	v_readlane_b32 s51, v251, 34
	v_readlane_b32 s52, v251, 35
	v_readlane_b32 s53, v251, 36
	v_readlane_b32 s54, v251, 37
	v_readlane_b32 s55, v251, 38
	v_readlane_b32 s58, v251, 41
	v_readlane_b32 s59, v251, 42
	v_readlane_b32 s60, v251, 43
	v_readlane_b32 s61, v251, 44
	v_readlane_b32 s62, v251, 45
	v_readlane_b32 s63, v251, 46

.LBB0_468:
	s_or_b64 exec, exec, s[8:9]
	v_add_u32_e32 v11, 0x35400, v1
	v_ashrrev_i32_e32 v15, 31, v11
	v_lshrrev_b32_e32 v17, 15, v15
	v_lshrrev_b32_e32 v15, 21, v15
	v_add_u32_e32 v15, v11, v15
	v_add_u32_e32 v17, v11, v17
	v_ashrrev_i32_e32 v15, 11, v15
	v_ashrrev_i32_e32 v22, 17, v17
	v_lshrrev_b32_e32 v17, 26, v15
	v_add_u32_e32 v17, v15, v17
	v_and_b32_e32 v17, 0xffffffc0, v17
	v_sub_u32_e32 v24, v15, v17
	v_mul_i32_i24_e32 v15, 0x800, v15
	s_mov_b32 s8, 0x4ac00
	v_sub_u32_e32 v26, v11, v15
	v_cmp_gt_i32_e32 vcc, s8, v1
	v_mov_b32_e32 v15, 0
	s_and_saveexec_b64 s[8:9], vcc
	s_cbranch_execz .LBB0_476
	v_cmp_lt_i32_e32 vcc, 3, v24
	s_and_saveexec_b64 s[10:11], vcc
	s_xor_b64 s[10:11], exec, s[10:11]
	s_cbranch_execz .LBB0_473
	v_cmp_gt_u32_e32 vcc, 36, v24
	v_mov_b32_e32 v15, 0
	s_and_saveexec_b64 s[12:13], vcc
	s_cbranch_execz .LBB0_472
	v_ashrrev_i32_e32 v23, 31, v22
	v_readlane_b32 s48, v251, 31
	v_ashrrev_i32_e32 v27, 31, v26
	v_lshlrev_b64 v[30:31], 18, v[22:23]
	v_readlane_b32 s56, v251, 39
	v_readlane_b32 s57, v251, 40
	v_lshlrev_b64 v[32:33], 7, v[26:27]
	v_mov_b32_e32 v25, v3
	v_lshl_add_u64 v[30:31], s[56:57], 0, v[30:31]
	v_lshl_add_u64 v[30:31], v[30:31], 0, v[32:33]
	v_lshl_add_u64 v[30:31], v[24:25], 2, v[30:31]
	global_load_dword v15, v[30:31], off offset:-16
	v_readlane_b32 s49, v251, 32
	v_readlane_b32 s50, v251, 33
	v_readlane_b32 s51, v251, 34
	v_readlane_b32 s52, v251, 35
	v_readlane_b32 s53, v251, 36
	v_readlane_b32 s54, v251, 37
	v_readlane_b32 s55, v251, 38
	v_readlane_b32 s58, v251, 41
	v_readlane_b32 s59, v251, 42
	v_readlane_b32 s60, v251, 43
	v_readlane_b32 s61, v251, 44
	v_readlane_b32 s62, v251, 45
	v_readlane_b32 s63, v251, 46

.LBB0_476:
	s_or_b64 exec, exec, s[8:9]
	v_ashrrev_i32_e32 v30, 8, v8
	v_ashrrev_i32_e32 v31, 31, v30
	v_lshlrev_b64 v[4:5], 7, v[4:5]
	v_lshrrev_b32_e32 v17, 4, v8
	v_lshlrev_b32_e32 v2, 2, v2
	v_lshl_add_u64 v[4:5], v[30:31], 4, v[4:5]
	v_ashrrev_i32_e32 v32, 5, v6
	v_sub_u32_e32 v2, v28, v2
	v_and_or_b32 v4, v17, 15, v4
	v_readlane_b32 s8, v253, 38
	v_and_b32_e32 v2, 32, v2
	v_ashrrev_i32_e32 v33, 31, v32
	v_lshlrev_b64 v[4:5], 12, v[4:5]
	v_readlane_b32 s9, v253, 39
	v_and_or_b32 v2, v6, 31, v2
	v_lshlrev_b64 v[30:31], 11, v[32:33]
	v_lshl_add_u64 v[4:5], s[8:9], 0, v[4:5]
	s_waitcnt vmcnt(0)
	v_bfe_u32 v11, v7, 16, 1
	v_and_b32_e32 v8, 7, v8
	v_lshl_add_u64 v[4:5], v[4:5], 0, v[30:31]
	v_lshlrev_b32_e32 v2, 4, v2
	v_add3_u32 v11, v7, v11, s33
	v_lshl_add_u64 v[4:5], v[4:5], 0, v[2:3]
	v_lshlrev_b32_e32 v2, 1, v8
	v_lshl_add_u64 v[4:5], v[4:5], 0, v[2:3]
	v_and_b32_e32 v2, 0xffff0000, v11
	v_sub_f32_e32 v2, v7, v2
	v_bfe_u32 v6, v2, 16, 1
	s_mov_b32 s8, 0x6e400
	v_add3_u32 v2, v2, v6, s33
	v_cmp_gt_i32_e32 vcc, s8, v1
	global_store_short_d16_hi v[4:5], v11, off
	global_store_short_d16_hi v[4:5], v2, off offset:1024
	s_and_saveexec_b64 s[8:9], vcc
	s_cbranch_execz .LBB0_478
	v_lshlrev_b32_e32 v5, 2, v14
	v_ashrrev_i32_e32 v4, 8, v14
	v_and_b32_e32 v5, 32, v5
	v_ashrrev_i32_e32 v11, 31, v10
	v_bfe_u32 v2, v13, 16, 1
	v_ashrrev_i32_e32 v6, 5, v12
	v_and_or_b32 v12, v12, 31, v5
	v_ashrrev_i32_e32 v5, 31, v4
	v_lshlrev_b64 v[10:11], 7, v[10:11]
	v_add3_u32 v8, v13, v2, s33
	v_lshrrev_b32_e32 v2, 4, v14
	v_lshl_add_u64 v[4:5], v[4:5], 4, v[10:11]
	v_and_or_b32 v4, v2, 15, v4
	v_readlane_b32 s10, v253, 38
	v_ashrrev_i32_e32 v7, 31, v6
	v_lshlrev_b64 v[4:5], 12, v[4:5]
	v_readlane_b32 s11, v253, 39
	v_lshlrev_b64 v[6:7], 11, v[6:7]
	v_and_b32_e32 v17, 7, v14
	v_lshl_add_u64 v[4:5], s[10:11], 0, v[4:5]
	v_lshl_add_u64 v[4:5], v[4:5], 0, v[6:7]
	v_lshlrev_b32_e32 v2, 4, v12
	v_lshl_add_u64 v[4:5], v[4:5], 0, v[2:3]
	v_lshlrev_b32_e32 v2, 1, v17
	v_lshl_add_u64 v[4:5], v[4:5], 0, v[2:3]
	v_and_b32_e32 v2, 0xffff0000, v8
	v_sub_f32_e32 v2, v13, v2
	v_bfe_u32 v6, v2, 16, 1
	v_add3_u32 v2, v2, v6, s33
	global_store_short_d16_hi v[4:5], v8, off
	global_store_short_d16_hi v[4:5], v2, off offset:1024
.LBB0_478:
	s_or_b64 exec, exec, s[8:9]
	s_mov_b32 s8, 0x5c800
	v_cmp_gt_i32_e32 vcc, s8, v1
	s_and_saveexec_b64 s[8:9], vcc
	s_cbranch_execz .LBB0_480
	v_lshlrev_b32_e32 v5, 2, v20
	v_ashrrev_i32_e32 v4, 8, v20
	v_and_b32_e32 v5, 32, v5
	v_ashrrev_i32_e32 v17, 31, v16
	v_bfe_u32 v2, v9, 16, 1
	v_and_or_b32 v13, v18, 31, v5
	v_ashrrev_i32_e32 v5, 31, v4
	v_lshlrev_b64 v[10:11], 7, v[16:17]
	v_add3_u32 v8, v9, v2, s33
	v_lshrrev_b32_e32 v2, 4, v20
	v_lshl_add_u64 v[4:5], v[4:5], 4, v[10:11]
	v_ashrrev_i32_e32 v6, 5, v18
	v_and_or_b32 v4, v2, 15, v4
	v_readlane_b32 s10, v253, 38
	v_ashrrev_i32_e32 v7, 31, v6
	v_lshlrev_b64 v[4:5], 12, v[4:5]
	v_readlane_b32 s11, v253, 39
	v_lshlrev_b64 v[6:7], 11, v[6:7]
	v_and_b32_e32 v12, 7, v20
	v_lshl_add_u64 v[4:5], s[10:11], 0, v[4:5]
	v_lshl_add_u64 v[4:5], v[4:5], 0, v[6:7]
	v_lshlrev_b32_e32 v2, 4, v13
	v_lshl_add_u64 v[4:5], v[4:5], 0, v[2:3]
	v_lshlrev_b32_e32 v2, 1, v12
	v_lshl_add_u64 v[4:5], v[4:5], 0, v[2:3]
	v_and_b32_e32 v2, 0xffff0000, v8
	v_sub_f32_e32 v2, v9, v2
	v_bfe_u32 v6, v2, 16, 1
	v_add3_u32 v2, v2, v6, s33
	global_store_short_d16_hi v[4:5], v8, off
	global_store_short_d16_hi v[4:5], v2, off offset:1024
.LBB0_480:
	s_or_b64 exec, exec, s[8:9]
	s_mov_b32 s8, 0x4ac00
	v_cmp_gt_i32_e32 vcc, s8, v1
	s_and_saveexec_b64 s[8:9], vcc
	s_cbranch_execz .LBB0_445
	v_lshlrev_b32_e32 v5, 2, v26
	v_ashrrev_i32_e32 v4, 8, v26
	v_and_b32_e32 v5, 32, v5
	v_ashrrev_i32_e32 v23, 31, v22
	v_bfe_u32 v2, v15, 16, 1
	v_and_or_b32 v12, v24, 31, v5
	v_ashrrev_i32_e32 v5, 31, v4
	v_lshlrev_b64 v[8:9], 7, v[22:23]
	v_add3_u32 v10, v15, v2, s33
	v_lshrrev_b32_e32 v2, 4, v26
	v_lshl_add_u64 v[4:5], v[4:5], 4, v[8:9]
	v_ashrrev_i32_e32 v6, 5, v24
	v_and_or_b32 v4, v2, 15, v4
	v_readlane_b32 s10, v253, 38
	v_ashrrev_i32_e32 v7, 31, v6
	v_lshlrev_b64 v[4:5], 12, v[4:5]
	v_readlane_b32 s11, v253, 39
	v_lshlrev_b64 v[6:7], 11, v[6:7]
	v_and_b32_e32 v11, 7, v26
	v_lshl_add_u64 v[4:5], s[10:11], 0, v[4:5]
	v_lshl_add_u64 v[4:5], v[4:5], 0, v[6:7]
	v_lshlrev_b32_e32 v2, 4, v12
	v_lshl_add_u64 v[4:5], v[4:5], 0, v[2:3]
	v_lshlrev_b32_e32 v2, 1, v11
	v_lshl_add_u64 v[4:5], v[4:5], 0, v[2:3]
	v_and_b32_e32 v2, 0xffff0000, v10
	v_sub_f32_e32 v2, v15, v2
	v_bfe_u32 v6, v2, 16, 1
	v_add3_u32 v2, v2, v6, s33
	global_store_short_d16_hi v[4:5], v10, off
	global_store_short_d16_hi v[4:5], v2, off offset:1024
	s_branch .LBB0_445
